# GEMM phase prologues: second staging group issued with the first (one wait of vmcnt(8)) in all six GEMM phases
# baseline (speedup 1.0000x reference)
.LBB0_219:
	s_add_i32 s17, s13, 1
	s_sext_i32_i8 s15, s12
	s_and_b64 s[12:13], s[18:19], exec
	s_cselect_b32 s80, 0, s17
	s_cselect_b32 s78, s15, s9
	s_cselect_b32 s79, s14, s16
	s_cselect_b32 s9, 0, 4
	s_add_u32 s67, s10, 0x17d00000
	s_addc_u32 s68, s11, 0
	s_add_u32 s69, s10, 0x28500000
	s_mov_b64 s[12:13], 0x80
	s_addc_u32 s70, s11, 0
	s_add_i32 m0, s50, 0x18000
	v_lshl_add_u64 v[8:9], v[8:9], 0, s[12:13]
	global_load_lds_dwordx4 v[8:9], off
	v_lshl_add_u64 v[6:7], v[6:7], 0, s[12:13]
	s_add_i32 m0, s50, 0x1a000
	s_add_i32 s71, s50, 0x8000
	global_load_lds_dwordx4 v[6:7], off
	v_lshl_add_u64 v[6:7], v[10:11], 0, s[12:13]
	s_mov_b32 m0, s71
	s_add_i32 s72, s50, 0xa000
	global_load_lds_dwordx4 v[6:7], off
	v_lshl_add_u64 v[6:7], v[12:13], 0, s[12:13]
	s_mov_b32 m0, s72
	v_lshl_add_u64 v[4:5], v[4:5], 0, s[12:13]
	global_load_lds_dwordx4 v[6:7], off
	s_add_i32 m0, s50, 0x1c000
	v_lshl_add_u64 v[2:3], v[2:3], 0, s[12:13]
	global_load_lds_dwordx4 v[4:5], off
	s_add_i32 m0, s50, 0x1e000
	s_lshl_b32 s10, s22, 13
	global_load_lds_dwordx4 v[2:3], off
	s_waitcnt vmcnt(8)
	s_barrier
	v_lshrrev_b32_e32 v3, 1, v14
	v_and_b32_e32 v3, 24, v3
	v_and_b32_e32 v2, 15, v14
	v_lshlrev_b32_e32 v4, 1, v3
	v_lshl_or_b32 v201, s22, 6, v2
	v_lshl_or_b32 v2, v2, 6, v4
	v_lshlrev_b32_e32 v4, 2, v14
	v_and_b32_e32 v4, 32, v4
	v_bitop3_b32 v5, v2, s10, v4 bitop3:0xde
	s_lshl_b32 s10, s21, 5
	s_and_b32 s10, s10, 0x60
	s_lshl_b32 s11, s10, 7
	v_bitop3_b32 v202, v2, s11, v4 bitop3:0xde
	v_lshlrev_b32_e32 v2, 14, v19
	v_and_b32_e32 v2, 0xffff8000, v2
	v_or_b32_e32 v203, s10, v3
	v_lshl_add_u32 v2, v20, 11, v2
	v_and_b32_e32 v3, 1, v19
	v_lshl_or_b32 v2, v3, 6, v2
	v_lshlrev_b32_sdwa v3, v17, sext(v21) dst_sel:DWORD dst_unused:UNUSED_PAD src0_sel:DWORD src1_sel:WORD_0
	v_add3_u32 v184, v2, v3, s66
	v_lshlrev_b32_e32 v2, 14, v15
	v_and_b32_e32 v2, 0xffff8000, v2
	v_lshl_add_u32 v2, v16, 11, v2
	v_and_b32_e32 v3, 1, v15
	v_lshl_or_b32 v2, v3, 6, v2
	v_lshlrev_b32_sdwa v3, v17, sext(v18) dst_sel:DWORD dst_unused:UNUSED_PAD src0_sel:DWORD src1_sel:WORD_0
	s_waitcnt vmcnt(6)
	v_add3_u32 v186, v2, v3, s66
	v_cndmask_b32_e64 v2, 0, 1, s[4:5]
	s_cmpk_lt_u32 s20, 0x100
	v_cmp_ne_u32_e64 s[4:5], 1, v2
	v_add_u32_e32 v2, 0, v202
	s_cselect_b64 s[14:15], -1, 0
	v_mov_b32_e32 v185, v183
	v_mov_b32_e32 v187, v183
	v_add_u32_e32 v204, 0x10000, v2
	v_add_u32_e32 v205, 0x14000, v2
	v_add_u32_e32 v206, 0, v5
	s_mov_b64 s[16:17], 0x40000
	s_mov_b64 s[18:19], 0x48000
	s_mov_b32 s73, 0x48000
	s_mov_b64 s[20:21], 0x50000
	s_mov_b32 s74, 0x50000
	s_mov_b64 s[22:23], 0x58000
	s_mov_b32 s38, 0
	s_barrier
	s_branch .LBB0_222

.LBB0_474:
	s_and_b32 s23, s64, 3
	s_add_u32 s47, s6, 0x36500000
	s_mov_b64 s[10:11], 0x80
	s_addc_u32 s48, s7, 0
	s_add_i32 m0, s42, 0x18000
	v_lshl_add_u64 v[8:9], v[8:9], 0, s[10:11]
	global_load_lds_dwordx4 v[8:9], off
	v_lshl_add_u64 v[6:7], v[6:7], 0, s[10:11]
	s_add_i32 m0, s42, 0x1a000
	s_add_i32 s49, s42, 0x8000
	global_load_lds_dwordx4 v[6:7], off
	v_lshl_add_u64 v[6:7], v[10:11], 0, s[10:11]
	s_mov_b32 m0, s49
	s_add_i32 s51, s42, 0xa000
	global_load_lds_dwordx4 v[6:7], off
	v_lshl_add_u64 v[6:7], v[12:13], 0, s[10:11]
	s_mov_b32 m0, s51
	v_lshl_add_u64 v[4:5], v[4:5], 0, s[10:11]
	global_load_lds_dwordx4 v[6:7], off
	s_add_i32 m0, s42, 0x1c000
	v_lshl_add_u64 v[2:3], v[2:3], 0, s[10:11]
	global_load_lds_dwordx4 v[4:5], off
	s_add_i32 m0, s42, 0x1e000
	s_lshl_b32 s5, s5, 5
	global_load_lds_dwordx4 v[2:3], off
	s_waitcnt vmcnt(8)
	s_barrier
	v_bfe_u32 v3, v14, 4, 2
	v_and_b32_e32 v2, 15, v14
	v_lshlrev_b32_e32 v4, 4, v3
	v_lshl_or_b32 v142, s12, 6, v2
	v_lshl_or_b32 v2, v2, 6, v4
	v_lshlrev_b32_e32 v4, 2, v14
	s_lshl_b32 s12, s12, 13
	v_and_b32_e32 v4, 32, v4
	s_and_b32 s5, s5, 0x60
	v_bitop3_b32 v5, v2, s12, v4 bitop3:0xde
	s_lshl_b32 s12, s5, 7
	v_bitop3_b32 v143, v2, s12, v4 bitop3:0xde
	v_lshlrev_b32_e32 v2, 15, v19
	v_and_b32_e32 v2, 0xffff0000, v2
	v_lshl_or_b32 v144, v3, 2, s5
	v_lshl_add_u32 v2, v20, 12, v2
	v_and_b32_e32 v3, 1, v19
	v_lshl_or_b32 v2, v3, 6, v2
	v_lshlrev_b32_sdwa v3, v17, sext(v21) dst_sel:DWORD dst_unused:UNUSED_PAD src0_sel:DWORD src1_sel:WORD_0
	v_add3_u32 v138, v2, v3, s14
	v_lshlrev_b32_e32 v2, 15, v15
	s_cmp_gt_i32 s38, 0
	v_and_b32_e32 v2, 0xffff0000, v2
	s_cselect_b64 s[16:17], -1, 0
	s_add_i32 s58, s38, -2
	v_lshl_add_u32 v2, v16, 12, v2
	v_and_b32_e32 v3, 1, v15
	s_waitcnt vmcnt(6)
	s_cmpk_lt_u32 s4, 0x100
	v_lshl_or_b32 v2, v3, 6, v2
	v_lshlrev_b32_sdwa v3, v17, sext(v18) dst_sel:DWORD dst_unused:UNUSED_PAD src0_sel:DWORD src1_sel:WORD_0
	s_cselect_b64 s[12:13], -1, 0
	v_add3_u32 v140, v2, v3, s14
	v_cndmask_b32_e64 v2, 0, 1, s[16:17]
	s_add_i32 s59, 0, 0x10000
	s_add_i32 s60, 0, 0x14000
	v_mov_b32_e32 v139, v135
	v_mov_b32_e32 v141, v135
	v_cmp_ne_u32_e64 s[4:5], 1, v2
	v_add_u32_e32 v145, s59, v143
	v_add_u32_e32 v146, s60, v143
	v_add_u32_e32 v147, 0, v5
	s_mov_b64 s[14:15], 0x40000
	s_mov_b32 s61, 0x40000
	s_mov_b64 s[16:17], 0x48000
	s_mov_b32 s63, 0x48000
	s_mov_b64 s[18:19], 0x50000
	s_mov_b32 s66, 0x50000
	s_mov_b64 s[20:21], 0x58000
	s_mov_b32 s67, 0x58000
	s_add_i32 s68, s42, 0xc000
	s_mov_b64 s[28:29], s[36:37]
	s_mov_b64 s[26:27], s[34:35]
	s_barrier
	s_branch .LBB0_477

.LBB0_492:
	s_and_b32 s31, s8, 3
	s_lshl_b32 s28, s59, 13
	s_lshl_b32 s29, s31, 12
	s_add_u32 s8, s6, 0x28500000
	s_addc_u32 s9, s7, 0
	s_add_u32 s10, s6, 0xf500000
	s_addc_u32 s11, s7, 0
	s_add_u32 s12, s6, 0x13500000
	s_addc_u32 s13, s7, 0
	s_add_u32 s69, s6, 0x200000
	s_addc_u32 s70, s7, 0
	s_add_u32 s14, s6, 0x7ca000
	s_addc_u32 s15, s7, 0
	s_add_u32 s16, s6, 0x7cb000
	s_addc_u32 s17, s7, 0
	s_add_u32 s18, s6, 0x7c8000
	s_addc_u32 s19, s7, 0
	s_add_u32 s20, s6, 0x7cc000
	s_addc_u32 s21, s7, 0
	s_add_u32 s22, s6, 0x7cd000
	s_addc_u32 s23, s7, 0
	s_add_u32 s24, s6, 0x7c9000
	s_addc_u32 s25, s7, 0
	s_add_u32 s71, s6, 0x420000
	s_mov_b64 s[26:27], 0x80
	s_addc_u32 s72, s7, 0
	s_add_i32 m0, s63, 0x18000
	v_lshl_add_u64 v[8:9], v[8:9], 0, s[26:27]
	global_load_lds_dwordx4 v[8:9], off
	v_lshl_add_u64 v[6:7], v[6:7], 0, s[26:27]
	s_add_i32 m0, s63, 0x1a000
	s_add_i32 s73, s63, 0x8000
	global_load_lds_dwordx4 v[6:7], off
	v_lshl_add_u64 v[6:7], v[12:13], 0, s[26:27]
	s_mov_b32 m0, s73
	s_add_i32 s74, s63, 0xa000
	global_load_lds_dwordx4 v[6:7], off
	v_lshl_add_u64 v[6:7], v[10:11], 0, s[26:27]
	s_mov_b32 m0, s74
	v_lshl_add_u64 v[4:5], v[4:5], 0, s[26:27]
	global_load_lds_dwordx4 v[6:7], off
	s_add_i32 m0, s63, 0x1c000
	v_lshl_add_u64 v[2:3], v[2:3], 0, s[26:27]
	global_load_lds_dwordx4 v[4:5], off
	s_add_i32 m0, s63, 0x1e000
	v_and_b32_e32 v1, 15, v14
	global_load_lds_dwordx4 v[2:3], off
	s_waitcnt vmcnt(8)
	s_barrier
	v_and_b32_e32 v2, 48, v14
	v_lshl_or_b32 v1, v1, 6, v2
	v_lshlrev_b32_e32 v2, 2, v14
	v_and_b32_e32 v2, 32, v2
	v_and_b32_e32 v4, 1, v20
	v_bitop3_b32 v3, v1, s28, v2 bitop3:0xde
	v_bitop3_b32 v1, v1, s29, v2 bitop3:0xde
	v_add3_u32 v2, v21, v22, v23
	v_lshlrev_b32_e32 v4, 6, v4
	v_lshl_or_b32 v2, v2, 11, v4
	v_lshlrev_b32_e32 v4, 1, v24
	v_add3_u32 v158, v2, v4, s30
	v_and_b32_e32 v4, 1, v15
	v_add3_u32 v2, v16, v17, v18
	v_lshlrev_b32_e32 v4, 6, v4
	s_waitcnt vmcnt(6)
	s_cmp_gt_i32 s51, 0
	v_lshl_or_b32 v2, v2, 11, v4
	v_lshlrev_b32_e32 v4, 1, v19
	s_cselect_b64 s[28:29], -1, 0
	v_lshl_add_u64 v[160:161], v[158:159], 0, s[26:27]
	v_add3_u32 v158, v2, v4, s30
	s_add_i32 s78, 0, 0x10000
	s_add_i32 s79, 0, 0x14000
	v_mov_b32_e32 v153, v159
	v_mov_b32_e32 v145, v159
	s_add_i32 s75, s51, -2
	s_lshl_b32 s76, s31, 4
	s_lshl_b32 s77, s59, 18
	v_lshl_add_u64 v[162:163], v[158:159], 0, s[26:27]
	v_add_u32_e32 v220, s78, v1
	v_add_u32_e32 v221, s79, v1
	v_add_u32_e32 v222, 0, v3
	v_mov_b32_e32 v223, 1.0
	s_mov_b64 s[36:37], s[46:47]
	s_mov_b64 s[34:35], s[44:45]
	s_barrier
	s_branch .LBB0_494

.LBB0_667:
	s_add_u32 s10, s6, 0xf500000
	s_mov_b64 s[12:13], 0x80
	s_addc_u32 s11, s7, 0
	s_add_i32 m0, s23, 0x18000
	v_lshl_add_u64 v[8:9], v[8:9], 0, s[12:13]
	global_load_lds_dwordx4 v[8:9], off
	v_lshl_add_u64 v[6:7], v[6:7], 0, s[12:13]
	s_add_i32 m0, s23, 0x1a000
	s_add_i32 s62, s23, 0x8000
	global_load_lds_dwordx4 v[6:7], off
	v_lshl_add_u64 v[6:7], v[10:11], 0, s[12:13]
	s_mov_b32 m0, s62
	s_add_i32 s63, s23, 0xa000
	global_load_lds_dwordx4 v[6:7], off
	v_lshl_add_u64 v[6:7], v[12:13], 0, s[12:13]
	s_mov_b32 m0, s63
	v_lshl_add_u64 v[4:5], v[4:5], 0, s[12:13]
	global_load_lds_dwordx4 v[6:7], off
	s_add_i32 m0, s23, 0x1c000
	v_lshl_add_u64 v[2:3], v[2:3], 0, s[12:13]
	global_load_lds_dwordx4 v[4:5], off
	s_add_i32 m0, s23, 0x1e000
	s_lshl_b32 s6, s16, 13
	global_load_lds_dwordx4 v[2:3], off
	s_waitcnt vmcnt(8)
	s_barrier
	v_lshrrev_b32_e32 v3, 1, v15
	v_and_b32_e32 v3, 24, v3
	v_and_b32_e32 v2, 15, v15
	v_lshlrev_b32_e32 v4, 1, v3
	v_lshl_or_b32 v199, s16, 6, v2
	v_lshl_or_b32 v2, v2, 6, v4
	v_lshlrev_b32_e32 v4, 2, v15
	v_and_b32_e32 v4, 32, v4
	v_bitop3_b32 v5, v2, s6, v4 bitop3:0xde
	s_lshl_b32 s6, s15, 5
	s_and_b32 s6, s6, 0x60
	s_lshl_b32 s7, s6, 7
	v_bitop3_b32 v200, v2, s7, v4 bitop3:0xde
	v_lshlrev_b32_e32 v2, 14, v19
	v_and_b32_e32 v2, 0xffff8000, v2
	v_or_b32_e32 v201, s6, v3
	v_lshl_add_u32 v2, v20, 11, v2
	v_and_b32_e32 v3, 1, v19
	v_lshl_or_b32 v2, v3, 6, v2
	v_lshlrev_b32_sdwa v3, v17, sext(v21) dst_sel:DWORD dst_unused:UNUSED_PAD src0_sel:DWORD src1_sel:WORD_0
	v_add3_u32 v182, v2, v3, s24
	v_lshlrev_b32_e32 v2, 14, v14
	s_cmp_gt_i32 s3, 0
	v_and_b32_e32 v2, 0xffff8000, v2
	s_sext_i32_i8 s70, s14
	s_cselect_b64 s[14:15], -1, 0
	s_cmpk_lt_u32 s5, 0x100
	v_lshl_add_u32 v2, v16, 11, v2
	v_and_b32_e32 v3, 1, v14
	s_waitcnt vmcnt(6)
	s_cselect_b64 s[16:17], -1, 0
	s_cmp_eq_u32 s3, 2
	v_lshl_or_b32 v2, v3, 6, v2
	v_lshlrev_b32_sdwa v3, v17, sext(v18) dst_sel:DWORD dst_unused:UNUSED_PAD src0_sel:DWORD src1_sel:WORD_0
	s_cselect_b64 s[18:19], -1, 0
	s_cmp_gt_u32 s3, 2
	v_add3_u32 v184, v2, v3, s24
	v_add_u32_e32 v2, 0, v200
	s_cselect_b64 s[20:21], -1, 0
	v_mov_b32_e32 v183, v179
	v_mov_b32_e32 v185, v179
	v_add_u32_e32 v202, 0x10000, v2
	v_add_u32_e32 v203, 0x14000, v2
	v_add_u32_e32 v204, 0, v5
	s_add_i32 s66, s23, 0xc000
	s_add_i32 s67, s23, 0xe000
	s_mov_b32 s5, 0
	s_mov_b64 s[28:29], s[34:35]
	s_mov_b64 s[30:31], s[36:37]
	s_barrier
	s_branch .LBB0_670

.LBB0_869:
	s_mov_b64 s[82:83], 0x80
	s_add_i32 m0, s15, 0x18000
	v_lshl_add_u64 v[8:9], v[8:9], 0, s[82:83]
	global_load_lds_dwordx4 v[8:9], off
	v_lshl_add_u64 v[6:7], v[6:7], 0, s[82:83]
	s_add_i32 m0, s15, 0x1a000
	s_add_i32 s23, s15, 0x8000
	global_load_lds_dwordx4 v[6:7], off
	v_lshl_add_u64 v[6:7], v[10:11], 0, s[82:83]
	s_mov_b32 m0, s23
	s_add_i32 s24, s15, 0xa000
	global_load_lds_dwordx4 v[6:7], off
	v_lshl_add_u64 v[6:7], v[12:13], 0, s[82:83]
	s_mov_b32 m0, s24
	v_lshl_add_u64 v[4:5], v[4:5], 0, s[82:83]
	global_load_lds_dwordx4 v[6:7], off
	s_add_i32 m0, s15, 0x1c000
	v_lshl_add_u64 v[2:3], v[2:3], 0, s[82:83]
	global_load_lds_dwordx4 v[4:5], off
	s_add_i32 m0, s15, 0x1e000
	v_lshrrev_b32_e32 v16, 1, v14
	global_load_lds_dwordx4 v[2:3], off
	s_waitcnt vmcnt(8)
	s_barrier
	v_and_b32_e32 v16, 24, v16
	v_and_b32_e32 v15, 15, v14
	v_lshlrev_b32_e32 v17, 1, v16
	v_lshl_or_b32 v183, s6, 6, v15
	v_lshl_or_b32 v15, v15, 6, v17
	v_lshlrev_b32_e32 v17, 2, v14
	s_lshl_b32 s0, s6, 13
	v_and_b32_e32 v17, 32, v17
	v_bitop3_b32 v18, v15, s0, v17 bitop3:0xde
	s_lshl_b32 s0, s5, 5
	s_and_b32 s6, s0, 0x60
	s_lshl_b32 s0, s6, 7
	s_cmp_lt_i32 s5, 4
	s_cselect_b64 s[84:85], -1, 0
	s_and_b32 s5, s4, 0xffffffc0
	v_bitop3_b32 v185, v15, s0, v17 bitop3:0xde
	s_movk_i32 s0, 0xffc0
	v_mov_b32_e32 v2, s4
	s_cmp_gt_i32 s12, 0
	v_bfi_b32 v211, s0, v2, v14
	s_cselect_b64 s[0:1], -1, 0
	s_cmpk_lt_u32 s4, 0x100
	s_cselect_b64 s[86:87], -1, 0
	s_cmp_eq_u32 s12, 2
	s_cselect_b64 s[88:89], -1, 0
	s_cmp_gt_u32 s12, 2
	s_waitcnt vmcnt(6)
	s_cselect_b64 s[90:91], -1, 0
	s_lshl_b32 s4, s5, 2
	s_add_i32 s25, s4, 0
	v_cndmask_b32_e64 v2, 0, 1, s[0:1]
	v_add_u32_e32 v3, 0, v185
	s_add_i32 s25, s25, 0x20560
	v_or_b32_e32 v212, s6, v16
	v_add_u32_e32 v213, 0x10000, v3
	v_add_u32_e32 v214, 0x14000, v3
	v_add_u32_e32 v215, 0, v18
	s_mov_b32 s26, 0xc3e00000
	v_cmp_ne_u32_e64 s[36:37], 1, v2
	s_add_i32 s27, s15, 0xc000
	v_mov_b32_e32 v216, 0x43e00000
	s_mov_b32 s6, 0
	s_barrier
	s_branch .LBB0_872

.LBB0_976:
	s_mov_b64 s[54:55], 0x80
	s_add_i32 m0, s15, 0x18000
	v_lshl_add_u64 v[10:11], v[10:11], 0, s[54:55]
	global_load_lds_dwordx4 v[10:11], off
	v_lshl_add_u64 v[8:9], v[8:9], 0, s[54:55]
	s_add_i32 m0, s15, 0x1a000
	s_add_i32 s26, s15, 0x8000
	global_load_lds_dwordx4 v[8:9], off
	v_lshl_add_u64 v[8:9], v[12:13], 0, s[54:55]
	s_mov_b32 m0, s26
	s_add_i32 s27, s15, 0xa000
	global_load_lds_dwordx4 v[8:9], off
	v_lshl_add_u64 v[6:7], v[6:7], 0, s[54:55]
	s_mov_b32 m0, s27
	v_lshl_add_u64 v[4:5], v[4:5], 0, s[54:55]
	global_load_lds_dwordx4 v[6:7], off
	s_add_i32 m0, s15, 0x1c000
	v_lshl_add_u64 v[2:3], v[2:3], 0, s[54:55]
	global_load_lds_dwordx4 v[4:5], off
	s_add_i32 m0, s15, 0x1e000
	v_and_b32_e32 v23, 48, v15
	global_load_lds_dwordx4 v[2:3], off
	s_waitcnt vmcnt(8)
	s_barrier
	v_lshlrev_b32_e32 v24, 6, v15
	s_movk_i32 s7, 0x3c0
	v_lshlrev_b32_e32 v15, 2, v15
	s_and_b32 s5, s5, 3
	s_lshl_b32 s25, s6, 6
	s_lshl_b32 s6, s6, 13
	v_and_or_b32 v23, v24, s7, v23
	v_and_b32_e32 v15, 32, v15
	v_lshlrev_b32_e32 v2, 12, v16
	v_bitop3_b32 v24, v23, s6, v15 bitop3:0xde
	s_lshl_b32 s6, s5, 12
	v_and_b32_e32 v2, 0xffffe000, v2
	v_bitop3_b32 v199, v23, s6, v15 bitop3:0xde
	s_and_b32 s6, s11, 0xffffffc0
	v_lshl_add_u32 v2, v18, 9, v2
	v_and_b32_e32 v3, 1, v16
	s_cmp_gt_i32 s10, 0
	v_lshl_or_b32 v2, v3, 6, v2
	v_lshlrev_b32_sdwa v3, v17, sext(v19) dst_sel:DWORD dst_unused:UNUSED_PAD src0_sel:DWORD src1_sel:WORD_0
	s_cselect_b64 s[76:77], -1, 0
	s_lshl_b32 s28, s5, 6
	v_add3_u32 v182, v2, v3, s4
	v_lshlrev_b32_e32 v2, 12, v20
	s_cmp_eq_u32 s10, 2
	v_and_b32_e32 v2, 0xffffe000, v2
	s_cselect_b64 s[80:81], -1, 0
	s_cmp_gt_u32 s10, 2
	v_lshl_add_u32 v2, v21, 9, v2
	v_and_b32_e32 v3, 1, v20
	s_waitcnt vmcnt(6)
	s_cselect_b64 s[82:83], -1, 0
	s_lshl_b32 s5, s6, 2
	v_lshl_or_b32 v2, v3, 6, v2
	v_lshlrev_b32_sdwa v3, v17, sext(v22) dst_sel:DWORD dst_unused:UNUSED_PAD src0_sel:DWORD src1_sel:WORD_0
	s_add_i32 s29, s5, 0
	v_add3_u32 v184, v2, v3, s4
	v_add_u32_e32 v2, 0, v199
	v_or_b32_e32 v200, s6, v14
	s_add_i32 s29, s29, 0x20560
	v_mov_b32_e32 v183, v175
	v_mov_b32_e32 v185, v175
	v_add_u32_e32 v201, 0x10000, v2
	v_add_u32_e32 v202, 0x14000, v2
	v_add_u32_e32 v203, 0, v24
	s_mov_b32 s89, 0xc3e00000
	v_mov_b32_e32 v204, 0x43e00000
	s_mov_b32 s16, 0
	s_barrier
	s_branch .LBB0_978
